# stack + dead SGPR-reload removal inside the mLSTM scan loop (71 v_readlane replaced by short s_nop runs), size-matched
# speedup vs baseline: 1.0119x; 1.0119x over previous
.LBB0_418:
	s_cmp_lt_u32 s7, 3
	s_cselect_b32 s11, s28, s11
	s_movk_i32 s0, 0xfff
	v_add_u32_e32 v34, s11, v124
	s_cselect_b32 s28, 0xff, s0
	v_sub_u32_e32 v35, s28, v34
	v_cndmask_b32_e64 v34, v35, v34, s[2:3]
	s_cselect_b32 s29, s45, s48
	v_add_u32_e32 v34, s29, v34
	v_ashrrev_i32_e32 v35, 31, v34
	v_lshlrev_b64 v[34:35], 12, v[34:35]
	v_lshl_add_u64 v[62:63], v[112:113], 0, v[34:35]
	global_load_dwordx4 v[34:37], v[62:63], off
	global_load_dwordx4 v[38:41], v[62:63], off offset:128
	global_load_dwordx4 v[42:45], v[62:63], off offset:2048
	global_load_dwordx4 v[46:49], v[62:63], off offset:2176
	global_load_dwordx4 v[50:53], v[62:63], off offset:256
	global_load_dwordx4 v[54:57], v[62:63], off offset:384
	global_load_dwordx4 v[58:61], v[62:63], off offset:2304
	s_nop 0
	global_load_dwordx4 v[62:65], v[62:63], off offset:2432
	v_mov_b64_e32 v[90:91], v[94:95]
	v_mov_b64_e32 v[92:93], v[96:97]
	s_and_saveexec_b64 s[0:1], s[4:5]
	s_cbranch_execz .LBB0_420
	v_add_u32_e32 v90, s11, v125
	v_sub_u32_e32 v91, s28, v90
	v_readlane_b32 s12, v255, 7
	v_cndmask_b32_e64 v90, v91, v90, s[2:3]
	v_readlane_b32 s13, v255, 8
	v_add_u32_e32 v92, s29, v90
	s_movk_i32 s11, 0x2800
	v_mov_b64_e32 v[90:91], s[12:13]
	v_readlane_b32 s12, v255, 40
	v_mad_i64_i32 v[90:91], s[28:29], v92, s11, v[90:91]
	s_mov_b32 s43, s41
	s_nop 0
	v_lshl_add_u64 v[90:91], v[90:91], 0, s[42:43]
	s_mov_b32 s13, s41
	v_lshl_add_u64 v[90:91], v[90:91], 0, s[12:13]
	v_mov_b32_e32 v115, v107
	v_lshl_add_u64 v[90:91], v[90:91], 0, v[114:115]
	v_add_co_u32_e32 v90, vcc, 0x1000, v90
	s_mov_b32 s28, s12
	s_nop 0
	v_addc_co_u32_e32 v91, vcc, 0, v91, vcc
	global_load_dwordx4 v[90:93], v[90:91], off
	v_writelane_b32 v255, s28, 40
	s_nop 1
	v_writelane_b32 v255, s29, 41

.LBB0_422:
	s_ashr_i32 s11, s51, 16
	s_bfe_u32 s92, s51, 0x5000b
	v_readlane_b32 s76, v254, 36
	s_cmp_eq_u32 s11, 1
	v_readlane_b32 s77, v254, 37
	v_readlane_b32 s78, v254, 38
	v_readlane_b32 s79, v254, 39
	s_nop 3
	s_cselect_b32 s0, s76, s78
	s_cselect_b32 s1, s77, s79
	s_nop 0
	s_cmp_lt_u32 s51, 0x10000
	v_readlane_b32 s82, v254, 58
	v_readlane_b32 s83, v254, 59
	s_cselect_b32 s1, s83, s1
	s_cselect_b32 s0, s82, s0
	s_lshl_b32 s12, s92, 24
	s_add_u32 s28, s0, s12
	s_addc_u32 s29, s1, 0
	s_nop 6
	s_cmp_eq_u32 s92, 0
	s_cselect_b64 s[90:91], -1, 0
	s_nop 0
	v_readlane_b32 s78, v254, 54
	v_readlane_b32 s79, v254, 55
	s_and_b64 s[0:1], s[90:91], exec
	v_readlane_b32 s74, v254, 34
	v_readlane_b32 s75, v254, 35
	s_cselect_b32 s30, s74, s78
	s_cselect_b32 s31, s75, s79
	s_cmp_eq_u32 s11, 3
	s_cselect_b64 s[52:53], -1, 0
	s_and_b64 s[0:1], s[52:53], exec
	s_cselect_b32 s1, s31, s29
	s_cselect_b32 s0, s30, s28
	s_and_b32 s43, s46, 0x7e0
	s_and_b32 s98, s51, 0x7c0
	s_lshl_b32 s98, s98, 13
	s_lshl_b32 s40, s43, 2
	s_add_u32 s98, s98, s40
	s_add_u32 s100, s0, s98
	s_addc_u32 s101, s1, 0
	global_load_dwordx4 v[152:155], v250, s[100:101]
	v_add_u32_e32 v253, 0x2000, v250
	global_load_dwordx4 v[156:159], v253, s[100:101]
	v_add_u32_e32 v252, 0x4000, v250
	global_load_dwordx4 v[160:163], v252, s[100:101]
	v_add_u32_e32 v253, 0x6000, v250
	global_load_dwordx4 v[164:167], v253, s[100:101]
	v_add_u32_e32 v252, 0x8000, v250
	global_load_dwordx4 v[168:171], v252, s[100:101]
	v_add_u32_e32 v253, 0xa000, v250
	global_load_dwordx4 v[172:175], v253, s[100:101]
	v_add_u32_e32 v252, 0xc000, v250
	global_load_dwordx4 v[176:179], v252, s[100:101]
	v_add_u32_e32 v253, 0xe000, v250
	global_load_dwordx4 v[246:249], v253, s[100:101]
	s_cmp_lt_u32 s7, 30
	s_cselect_b64 s[94:95], -1, 0
	s_and_b64 s[0:1], s[94:95], exec
	s_cselect_b32 s0, s49, 0
	s_add_i32 s0, s0, s44
	s_lshl_b32 s0, s0, 3
	v_readlane_b32 s1, v255, 15
	s_add_i32 s28, s1, s0
	s_bfe_u32 s93, s28, 0x5000b
	s_ashr_i32 s57, s28, 16
	s_lshl_b32 s13, s93, 22
	s_cmp_eq_u32 s57, 3
	s_cselect_b64 s[96:97], -1, 0
	s_cmp_eq_u32 s93, 0
	s_cselect_b64 s[0:1], -1, 0
	s_lshl_b32 s34, s28, 5
	s_and_b32 s37, s34, 0x7e0
	s_and_b32 s36, s28, 0x7c0
	s_mov_b32 s38, s86
	s_cmp_gt_u32 s7, 29
	s_nop 4
	v_readlane_b32 s62, v254, 22
	s_nop 7
	s_cbranch_scc1 .LBB0_424
	v_readlane_b32 s80, v254, 36
	s_cmp_eq_u32 s57, 1
	v_readlane_b32 s81, v254, 37
	v_readlane_b32 s82, v254, 38
	v_readlane_b32 s83, v254, 39
	s_cselect_b32 s29, s80, s82
	s_cselect_b32 s30, s81, s83
	s_nop 0
	s_cmp_lt_u32 s28, 0x10000
	v_readlane_b32 s82, v254, 58
	v_readlane_b32 s83, v254, 59
	s_cselect_b32 s28, s83, s30
	s_cselect_b32 s29, s82, s29
	s_lshl_b32 s30, s13, 2
	s_nop 6
	s_add_u32 s30, s29, s30
	s_addc_u32 s31, s28, 0
	s_nop 0
	v_readlane_b32 s78, v254, 54
	v_readlane_b32 s79, v254, 55
	s_and_b64 s[28:29], s[0:1], exec
	v_readlane_b32 s74, v254, 34
	v_readlane_b32 s75, v254, 35
	s_cselect_b32 s60, s74, s78
	s_cselect_b32 vcc_lo, s75, s79
	s_and_b64 s[28:29], s[96:97], exec
	s_cselect_b32 s29, vcc_lo, s31
	s_cselect_b32 s28, s60, s30
	s_lshl_b32 s98, s36, 13
	s_lshl_b32 s40, s37, 2
	s_add_u32 s98, s98, s40
	s_add_u32 s100, s28, s98
	s_addc_u32 s101, s29, 0
	global_load_dwordx4 v[2:5], v250, s[100:101]
	v_add_u32_e32 v253, 0x2000, v250
	global_load_dwordx4 v[6:9], v253, s[100:101]
	v_add_u32_e32 v252, 0x4000, v250
	global_load_dwordx4 v[10:13], v252, s[100:101]
	v_add_u32_e32 v253, 0x6000, v250
	global_load_dwordx4 v[14:17], v253, s[100:101]
	v_add_u32_e32 v252, 0x8000, v250
	global_load_dwordx4 v[18:21], v252, s[100:101]
	v_add_u32_e32 v253, 0xa000, v250
	global_load_dwordx4 v[22:25], v253, s[100:101]
	v_add_u32_e32 v252, 0xc000, v250
	global_load_dwordx4 v[26:29], v252, s[100:101]
	v_add_u32_e32 v253, 0xe000, v250
	global_load_dwordx4 v[116:119], v253, s[100:101]
	s_nop 7
	v_readlane_b32 s62, v254, 22
	s_nop 7

.LBB0_455:
	s_lshl_b32 s7, s92, 22
	s_lshl_b32 s7, s7, 1
	s_add_u32 s7, s35, s7
	s_addc_u32 s28, s33, 0
	s_add_u32 s29, s56, s12
	s_addc_u32 s30, s39, 0
	s_cmp_eq_u32 s11, 2
	s_cselect_b32 s7, s7, s29
	s_cselect_b32 s30, s28, s30
	s_and_b64 s[28:29], s[90:91], exec
	s_mov_b32 s12, 0x2400000
	s_nop 0
	s_cselect_b32 s28, s12, 0x4300000
	v_readlane_b32 s86, v254, 42
	v_readlane_b32 s87, v254, 43
	s_add_u32 s31, s86, s28
	s_addc_u32 s60, s87, 0
	s_and_b64 s[28:29], s[52:53], exec
	s_cselect_b32 s29, s60, s30
	s_cselect_b32 s28, s31, s7
	s_lshl_b32 s7, s43, 1
	s_and_b32 s30, s46, 0x60
	s_lshl_b32 s31, s11, 7
	s_and_b32 s7, s7, 0xf00
	s_or_b32 s30, s31, s30
	s_add_i32 s30, s30, s7
	s_cmp_gt_i32 s11, 1
	s_cselect_b32 s7, s43, s30
	s_ashr_i32 s11, s7, 3
	s_andn2_b32 s11, s11, 31
	s_or_b32 s30, s11, s50
	s_ashr_i32 s31, s30, 31
	s_lshl_b64 s[30:31], s[30:31], 8
	s_and_b32 s7, s7, 0xe0
	s_or_b32 s7, s30, s7
	s_mov_b32 s100, s7
	s_mov_b32 s101, s31
	s_lshl_b64 s[100:101], s[100:101], 7
	s_add_u32 s100, s100, s28
	s_addc_u32 s101, s101, s29
	s_waitcnt vmcnt(1)
	v_cvt_pk_bf16_f32 v152, v152, v156
	v_cvt_pk_bf16_f32 v156, v153, v157
	v_cvt_pk_bf16_f32 v238, v154, v158
	v_cvt_pk_bf16_f32 v242, v155, v159
	v_cvt_pk_bf16_f32 v153, v160, v164
	v_cvt_pk_bf16_f32 v157, v161, v165
	v_cvt_pk_bf16_f32 v239, v162, v166
	v_cvt_pk_bf16_f32 v243, v163, v167
	v_cvt_pk_bf16_f32 v154, v168, v172
	v_cvt_pk_bf16_f32 v158, v169, v173
	v_cvt_pk_bf16_f32 v240, v170, v174
	v_cvt_pk_bf16_f32 v244, v171, v175
	v_cvt_pk_bf16_f32 v155, v176, v246
	v_cvt_pk_bf16_f32 v159, v177, v247
	v_cvt_pk_bf16_f32 v241, v178, v248
	v_cvt_pk_bf16_f32 v245, v179, v249
	global_store_dwordx4 v251, v[152:155], s[100:101]
	global_store_dwordx4 v251, v[156:159], s[100:101] offset:128
	global_store_dwordx4 v251, v[238:241], s[100:101] offset:256
	global_store_dwordx4 v251, v[242:245], s[100:101] offset:384
	s_andn2_b64 vcc, exec, s[94:95]
	s_mov_b32 s86, s38
	s_nop 4
	s_cbranch_vccnz .LBB0_410
	s_lshl_b32 s7, s13, 1
	s_add_u32 s7, s35, s7
	s_addc_u32 s11, s33, 0
	s_lshl_b32 s28, s93, 24
	s_add_u32 s28, s56, s28
	s_addc_u32 s29, s39, 0
	s_cmp_eq_u32 s57, 2
	s_cselect_b32 s7, s7, s28
	s_cselect_b32 s11, s11, s29
	s_and_b64 s[0:1], s[0:1], exec
	s_mov_b32 s0, 0x2400000
	s_nop 0
	s_cselect_b32 s0, s0, 0x4300000
	v_readlane_b32 s78, v254, 42
	v_readlane_b32 s79, v254, 43
	s_add_u32 s28, s78, s0
	s_addc_u32 s29, s79, 0
	s_and_b64 s[0:1], s[96:97], exec
	s_cselect_b32 s1, s29, s11
	s_cselect_b32 s0, s28, s7
	s_lshl_b32 s7, s37, 1
	s_and_b32 s11, s34, 0x60
	s_lshl_b32 s28, s57, 7
	s_and_b32 s7, s7, 0xf00
	s_or_b32 s11, s28, s11
	s_add_i32 s11, s11, s7
	s_cmp_gt_i32 s57, 1
	s_cselect_b32 s7, s37, s11
	s_ashr_i32 s11, s7, 3
	s_andn2_b32 s11, s11, 31
	s_lshr_b32 s28, s36, 6
	s_or_b32 s28, s11, s28
	s_ashr_i32 s29, s28, 31
	s_lshl_b64 s[28:29], s[28:29], 8
	s_and_b32 s7, s7, 0xe0
	s_or_b32 s7, s28, s7
	s_nop 4
	s_mov_b32 s100, s7
	s_mov_b32 s101, s29
	s_lshl_b64 s[100:101], s[100:101], 7
	s_add_u32 s100, s100, s0
	s_addc_u32 s101, s101, s1
	v_cvt_pk_bf16_f32 v2, v2, v6
	v_cvt_pk_bf16_f32 v6, v3, v7
	v_cvt_pk_bf16_f32 v238, v4, v8
	v_cvt_pk_bf16_f32 v242, v5, v9
	v_cvt_pk_bf16_f32 v3, v10, v14
	v_cvt_pk_bf16_f32 v7, v11, v15
	v_cvt_pk_bf16_f32 v239, v12, v16
	v_cvt_pk_bf16_f32 v243, v13, v17
	v_cvt_pk_bf16_f32 v4, v18, v22
	v_cvt_pk_bf16_f32 v8, v19, v23
	v_cvt_pk_bf16_f32 v240, v20, v24
	v_cvt_pk_bf16_f32 v244, v21, v25
	v_cvt_pk_bf16_f32 v5, v26, v116
	v_cvt_pk_bf16_f32 v9, v27, v117
	v_cvt_pk_bf16_f32 v241, v28, v118
	v_cvt_pk_bf16_f32 v245, v29, v119
	global_store_dwordx4 v251, v[2:5], s[100:101]
	global_store_dwordx4 v251, v[6:9], s[100:101] offset:128
	global_store_dwordx4 v251, v[238:241], s[100:101] offset:256
	global_store_dwordx4 v251, v[242:245], s[100:101] offset:384
	s_branch .LBB0_410
	s_nop 0
	s_nop 0
	s_nop 0
	s_nop 0
	s_nop 0
	s_nop 0
	s_nop 0
	s_nop 0
	s_nop 0
	s_nop 0
	s_nop 0
	s_nop 0
	s_nop 0
	s_nop 0
